# K/V block loads of the pipelined selected loop marked sc1
# speedup vs baseline: 1.0016x; 1.0002x over previous
.Lsel_pro_p3:
	s_cmp_lt_i32 s32, 0
	s_cbranch_scc1 .Lsel_pro_nol1
	s_lshl_b32 s2, s32, 15
	s_add_u32 s0, s90, s2
	s_addc_u32 s1, s91, 0
	global_load_dwordx4 v[124:127], v121, s[0:1] sc1
	s_add_u32 s0, s92, s2
	s_addc_u32 s1, s93, 0
	global_load_dwordx4 v[252:255], v121, s[0:1] sc1
	s_cmp_lt_i32 s81, 0
	s_cbranch_scc1 .Lsel_pro_nol1
	s_lshl_b32 s2, s81, 15
	s_add_u32 s0, s90, s2
	s_addc_u32 s1, s91, 0
	global_load_dwordx4 v[112:115], v121, s[0:1] sc1
	s_add_u32 s0, s92, s2
	s_addc_u32 s1, s93, 0
	global_load_dwordx4 v[116:119], v121, s[0:1] sc1

.Lsel_pro_w1:
	ds_write_b128 v250, v[124:127]
	ds_write_b128 v251, v[252:255] offset:18432
	s_cmp_lt_i32 s100, 0
	s_cbranch_scc1 .Lsel_pro_now1
	s_lshl_b32 s2, s100, 15
	s_add_u32 s0, s90, s2
	s_addc_u32 s1, s91, 0
	global_load_dwordx4 v[124:127], v121, s[0:1] sc1
	s_add_u32 s0, s92, s2
	s_addc_u32 s1, s93, 0
	global_load_dwordx4 v[252:255], v121, s[0:1] sc1

.Lsel_skipp_X_S:
	s_cmp_lt_i32 s3, 0
	s_cbranch_scc1 .Lsel_skipl_X_S
	s_lshl_b32 s2, s3, 15
	s_add_u32 s0, s90, s2
	s_addc_u32 s1, s91, 0
	global_load_dwordx4 v[112:115], v121, s[0:1] sc1
	s_add_u32 s0, s92, s2
	s_addc_u32 s1, s93, 0
	global_load_dwordx4 v[116:119], v121, s[0:1] sc1

.Lsel_skipp_Y_S:
	s_cmp_lt_i32 s3, 0
	s_cbranch_scc1 .Lsel_skipl_Y_S
	s_lshl_b32 s2, s3, 15
	s_add_u32 s0, s90, s2
	s_addc_u32 s1, s91, 0
	global_load_dwordx4 v[124:127], v121, s[0:1] sc1
	s_add_u32 s0, s92, s2
	s_addc_u32 s1, s93, 0
	global_load_dwordx4 v[252:255], v121, s[0:1] sc1
